# opt6 counters + IN1 epilogue: cos/sin quads of all 8 rows preloaded once per tile into dead VGPRs instead of 16 load+vmcnt(0) round trips
# speedup vs baseline: 1.1081x; 1.0121x over previous
.LBB0_1076:
	ds_read_b128 v[148:151], v158
	ds_read_b128 v[152:155], v158 offset:1024
	ds_read_b128 v[162:165], v158 offset:2048
	ds_read_b128 v[166:169], v158 offset:3072
	s_add_u32 s10, s8, 0xfffc0080
	s_addc_u32 s11, s9, -1
	s_cmp_eq_u32 s23, 12
	s_cselect_b32 s13, s1, s11
	s_cselect_b32 s12, s14, s10
	s_cselect_b32 s11, s15, s21
	s_cselect_b32 s10, s16, s17
	v_lshl_add_u64 v[202:203], s[8:9], 0, v[140:141]
	s_add_i32 m0, s29, 0xc000
	ds_read_b128 v[170:173], v159
	ds_read_b128 v[174:177], v159 offset:1024
	ds_read_b128 v[178:181], v159 offset:2048
	ds_read_b128 v[182:185], v159 offset:3072
	ds_read_b128 v[186:189], v159 offset:4096
	ds_read_b128 v[190:193], v159 offset:5120
	ds_read_b128 v[194:197], v159 offset:6144
	ds_read_b128 v[198:201], v159 offset:7168
	global_load_lds_dwordx4 v[202:203], off
	v_lshl_add_u64 v[202:203], s[8:9], 0, v[142:143]
	s_add_i32 m0, s29, 0xe000
	s_nop 0
	global_load_lds_dwordx4 v[202:203], off
	s_waitcnt lgkmcnt(8)
	s_barrier
	s_waitcnt lgkmcnt(0)
	s_setprio 1
	s_waitcnt lgkmcnt(0)
	v_mfma_f32_16x16x32_bf16 v[124:127], v[148:151], v[170:173], v[124:127]
	v_mfma_f32_16x16x32_bf16 v[120:123], v[162:165], v[170:173], v[120:123]
	v_mfma_f32_16x16x32_bf16 v[108:111], v[148:151], v[178:181], v[108:111]
	v_mfma_f32_16x16x32_bf16 v[104:107], v[162:165], v[178:181], v[104:107]
	v_mfma_f32_16x16x32_bf16 v[92:95], v[148:151], v[186:189], v[92:95]
	v_mfma_f32_16x16x32_bf16 v[88:91], v[162:165], v[186:189], v[88:91]
	v_mfma_f32_16x16x32_bf16 v[76:79], v[148:151], v[194:197], v[76:79]
	v_mfma_f32_16x16x32_bf16 v[72:75], v[162:165], v[194:197], v[72:75]
	v_mfma_f32_16x16x32_bf16 v[124:127], v[152:155], v[174:177], v[124:127]
	v_mfma_f32_16x16x32_bf16 v[120:123], v[166:169], v[174:177], v[120:123]
	v_mfma_f32_16x16x32_bf16 v[108:111], v[152:155], v[182:185], v[108:111]
	v_mfma_f32_16x16x32_bf16 v[104:107], v[166:169], v[182:185], v[104:107]
	v_mfma_f32_16x16x32_bf16 v[92:95], v[152:155], v[190:193], v[92:95]
	v_mfma_f32_16x16x32_bf16 v[88:91], v[166:169], v[190:193], v[88:91]
	v_mfma_f32_16x16x32_bf16 v[76:79], v[152:155], v[198:201], v[76:79]
	v_mfma_f32_16x16x32_bf16 v[72:75], v[166:169], v[198:201], v[72:75]
	s_setprio 0
	s_barrier
	s_add_i32 s38, s55, s45
	v_lshl_add_u64 v[218:219], s[10:11], 0, v[128:129]
	s_mov_b32 m0, s38
	ds_read_b128 v[202:205], v160
	ds_read_b128 v[206:209], v160 offset:1024
	ds_read_b128 v[210:213], v160 offset:2048
	ds_read_b128 v[214:217], v160 offset:3072
	global_load_lds_dwordx4 v[218:219], off
	v_lshl_add_u64 v[220:221], s[10:11], 0, v[130:131]
	s_add_i32 m0, s38, 0x2000
	s_nop 0
	global_load_lds_dwordx4 v[220:221], off
	s_barrier
	s_waitcnt lgkmcnt(0)
	s_setprio 1
	s_waitcnt lgkmcnt(0)
	v_mfma_f32_16x16x32_bf16 v[116:119], v[202:205], v[170:173], v[116:119]
	v_mfma_f32_16x16x32_bf16 v[112:115], v[210:213], v[170:173], v[112:115]
	v_mfma_f32_16x16x32_bf16 v[100:103], v[202:205], v[178:181], v[100:103]
	v_mfma_f32_16x16x32_bf16 v[96:99], v[210:213], v[178:181], v[96:99]
	v_mfma_f32_16x16x32_bf16 v[84:87], v[202:205], v[186:189], v[84:87]
	v_mfma_f32_16x16x32_bf16 v[80:83], v[210:213], v[186:189], v[80:83]
	v_mfma_f32_16x16x32_bf16 v[68:71], v[202:205], v[194:197], v[68:71]
	v_mfma_f32_16x16x32_bf16 v[64:67], v[210:213], v[194:197], v[64:67]
	v_mfma_f32_16x16x32_bf16 v[116:119], v[206:209], v[174:177], v[116:119]
	v_mfma_f32_16x16x32_bf16 v[112:115], v[214:217], v[174:177], v[112:115]
	v_mfma_f32_16x16x32_bf16 v[100:103], v[206:209], v[182:185], v[100:103]
	v_mfma_f32_16x16x32_bf16 v[96:99], v[214:217], v[182:185], v[96:99]
	v_mfma_f32_16x16x32_bf16 v[84:87], v[206:209], v[190:193], v[84:87]
	v_mfma_f32_16x16x32_bf16 v[80:83], v[214:217], v[190:193], v[80:83]
	v_mfma_f32_16x16x32_bf16 v[68:71], v[206:209], v[198:201], v[68:71]
	v_mfma_f32_16x16x32_bf16 v[64:67], v[214:217], v[198:201], v[64:67]
	s_setprio 0
	s_mov_b32 m0, s29
	v_lshl_add_u64 v[222:223], s[12:13], 0, v[128:129]
	s_barrier
	ds_read_b128 v[170:173], v159 offset:16384
	ds_read_b128 v[174:177], v159 offset:17408
	ds_read_b128 v[178:181], v159 offset:18432
	ds_read_b128 v[182:185], v159 offset:19456
	ds_read_b128 v[186:189], v159 offset:20480
	ds_read_b128 v[190:193], v159 offset:21504
	ds_read_b128 v[194:197], v159 offset:22528
	ds_read_b128 v[198:201], v159 offset:23552
	global_load_lds_dwordx4 v[222:223], off
	v_lshl_add_u64 v[224:225], s[12:13], 0, v[130:131]
	s_mov_b32 m0, s46
	s_nop 0
	global_load_lds_dwordx4 v[224:225], off
	s_barrier
	s_waitcnt lgkmcnt(0)
	s_setprio 1
	s_waitcnt lgkmcnt(0)
	v_mfma_f32_16x16x32_bf16 v[60:63], v[148:151], v[170:173], v[60:63]
	v_mfma_f32_16x16x32_bf16 v[56:59], v[162:165], v[170:173], v[56:59]
	v_mfma_f32_16x16x32_bf16 v[44:47], v[148:151], v[178:181], v[44:47]
	v_mfma_f32_16x16x32_bf16 v[40:43], v[162:165], v[178:181], v[40:43]
	v_mfma_f32_16x16x32_bf16 v[28:31], v[148:151], v[186:189], v[28:31]
	v_mfma_f32_16x16x32_bf16 v[24:27], v[162:165], v[186:189], v[24:27]
	v_mfma_f32_16x16x32_bf16 v[12:15], v[148:151], v[194:197], v[12:15]
	v_mfma_f32_16x16x32_bf16 v[8:11], v[162:165], v[194:197], v[8:11]
	v_mfma_f32_16x16x32_bf16 v[60:63], v[152:155], v[174:177], v[60:63]
	v_mfma_f32_16x16x32_bf16 v[56:59], v[166:169], v[174:177], v[56:59]
	v_mfma_f32_16x16x32_bf16 v[44:47], v[152:155], v[182:185], v[44:47]
	v_mfma_f32_16x16x32_bf16 v[40:43], v[166:169], v[182:185], v[40:43]
	v_mfma_f32_16x16x32_bf16 v[28:31], v[152:155], v[190:193], v[28:31]
	v_mfma_f32_16x16x32_bf16 v[24:27], v[166:169], v[190:193], v[24:27]
	v_mfma_f32_16x16x32_bf16 v[12:15], v[152:155], v[198:201], v[12:15]
	v_mfma_f32_16x16x32_bf16 v[8:11], v[166:169], v[198:201], v[8:11]
	s_setprio 0
	s_barrier
	s_add_u32 s38, s10, 0x40000
	s_addc_u32 s39, s11, 0
	s_add_i32 s40, s56, s45
	v_lshl_add_u64 v[148:149], s[38:39], 0, v[128:129]
	s_mov_b32 m0, s40
	s_nop 0
	global_load_lds_dwordx4 v[148:149], off
	v_lshl_add_u64 v[148:149], s[38:39], 0, v[130:131]
	s_add_i32 m0, s40, 0x2000
	s_nop 0
	global_load_lds_dwordx4 v[148:149], off
	s_waitcnt vmcnt(6)
	s_barrier
	s_setprio 1
	v_mfma_f32_16x16x32_bf16 v[52:55], v[202:205], v[170:173], v[52:55]
	v_mfma_f32_16x16x32_bf16 v[48:51], v[210:213], v[170:173], v[48:51]
	v_mfma_f32_16x16x32_bf16 v[36:39], v[202:205], v[178:181], v[36:39]
	v_mfma_f32_16x16x32_bf16 v[32:35], v[210:213], v[178:181], v[32:35]
	v_mfma_f32_16x16x32_bf16 v[20:23], v[202:205], v[186:189], v[20:23]
	v_mfma_f32_16x16x32_bf16 v[16:19], v[210:213], v[186:189], v[16:19]
	v_mfma_f32_16x16x32_bf16 v[4:7], v[202:205], v[194:197], v[4:7]
	v_mfma_f32_16x16x32_bf16 v[0:3], v[210:213], v[194:197], v[0:3]
	v_mfma_f32_16x16x32_bf16 v[52:55], v[206:209], v[174:177], v[52:55]
	v_mfma_f32_16x16x32_bf16 v[48:51], v[214:217], v[174:177], v[48:51]
	v_mfma_f32_16x16x32_bf16 v[36:39], v[206:209], v[182:185], v[36:39]
	v_mfma_f32_16x16x32_bf16 v[32:35], v[214:217], v[182:185], v[32:35]
	v_mfma_f32_16x16x32_bf16 v[20:23], v[206:209], v[190:193], v[20:23]
	v_mfma_f32_16x16x32_bf16 v[16:19], v[214:217], v[190:193], v[16:19]
	v_mfma_f32_16x16x32_bf16 v[4:7], v[206:209], v[198:201], v[4:7]
	v_mfma_f32_16x16x32_bf16 v[0:3], v[214:217], v[198:201], v[0:3]
	s_setprio 0
	s_add_i32 s38, 0, 0x18000
	v_add_u32_e32 v132, s38, v157
	s_barrier
	ds_read_b128 v[148:151], v132
	ds_read_b128 v[152:155], v132 offset:1024
	ds_read_b128 v[162:165], v132 offset:2048
	ds_read_b128 v[166:169], v132 offset:3072
	s_add_u32 s12, s12, 0x40000
	s_addc_u32 s13, s13, 0
	s_mov_b32 m0, s47
	v_lshl_add_u64 v[202:203], s[12:13], 0, v[128:129]
	ds_read_b128 v[170:173], v159 offset:32768
	ds_read_b128 v[174:177], v159 offset:33792
	ds_read_b128 v[178:181], v159 offset:34816
	ds_read_b128 v[182:185], v159 offset:35840
	ds_read_b128 v[186:189], v159 offset:36864
	ds_read_b128 v[190:193], v159 offset:37888
	ds_read_b128 v[194:197], v159 offset:38912
	ds_read_b128 v[198:201], v159 offset:39936
	global_load_lds_dwordx4 v[202:203], off
	v_lshl_add_u64 v[202:203], s[12:13], 0, v[130:131]
	s_mov_b32 m0, s48
	s_nop 0
	global_load_lds_dwordx4 v[202:203], off
	s_waitcnt lgkmcnt(8)
	s_barrier
	s_waitcnt lgkmcnt(0)
	s_setprio 1
	s_waitcnt lgkmcnt(0)
	v_mfma_f32_16x16x32_bf16 v[124:127], v[148:151], v[170:173], v[124:127]
	v_mfma_f32_16x16x32_bf16 v[120:123], v[162:165], v[170:173], v[120:123]
	v_mfma_f32_16x16x32_bf16 v[108:111], v[148:151], v[178:181], v[108:111]
	v_mfma_f32_16x16x32_bf16 v[104:107], v[162:165], v[178:181], v[104:107]
	v_mfma_f32_16x16x32_bf16 v[92:95], v[148:151], v[186:189], v[92:95]
	v_mfma_f32_16x16x32_bf16 v[88:91], v[162:165], v[186:189], v[88:91]
	v_mfma_f32_16x16x32_bf16 v[76:79], v[148:151], v[194:197], v[76:79]
	v_mfma_f32_16x16x32_bf16 v[72:75], v[162:165], v[194:197], v[72:75]
	v_mfma_f32_16x16x32_bf16 v[124:127], v[152:155], v[174:177], v[124:127]
	v_mfma_f32_16x16x32_bf16 v[120:123], v[166:169], v[174:177], v[120:123]
	v_mfma_f32_16x16x32_bf16 v[108:111], v[152:155], v[182:185], v[108:111]
	v_mfma_f32_16x16x32_bf16 v[104:107], v[166:169], v[182:185], v[104:107]
	v_mfma_f32_16x16x32_bf16 v[92:95], v[152:155], v[190:193], v[92:95]
	v_mfma_f32_16x16x32_bf16 v[88:91], v[166:169], v[190:193], v[88:91]
	v_mfma_f32_16x16x32_bf16 v[76:79], v[152:155], v[198:201], v[76:79]
	v_mfma_f32_16x16x32_bf16 v[72:75], v[166:169], v[198:201], v[72:75]
	s_setprio 0
	s_barrier
	s_add_i32 s12, 0, 0x1c000
	s_add_i32 s13, s38, s45
	v_add_u32_e32 v132, s12, v157
	v_lshl_add_u64 v[218:219], v[218:219], 0, s[2:3]
	s_mov_b32 m0, s13
	ds_read_b128 v[202:205], v132
	ds_read_b128 v[206:209], v132 offset:1024
	ds_read_b128 v[210:213], v132 offset:2048
	ds_read_b128 v[214:217], v132 offset:3072
	global_load_lds_dwordx4 v[218:219], off
	v_lshl_add_u64 v[218:219], v[220:221], 0, s[2:3]
	s_add_i32 m0, s13, 0x2000
	s_nop 0
	global_load_lds_dwordx4 v[218:219], off
	s_barrier
	s_waitcnt lgkmcnt(0)
	s_setprio 1
	s_waitcnt lgkmcnt(0)
	v_mfma_f32_16x16x32_bf16 v[116:119], v[202:205], v[170:173], v[116:119]
	v_mfma_f32_16x16x32_bf16 v[112:115], v[210:213], v[170:173], v[112:115]
	v_mfma_f32_16x16x32_bf16 v[100:103], v[202:205], v[178:181], v[100:103]
	v_mfma_f32_16x16x32_bf16 v[96:99], v[210:213], v[178:181], v[96:99]
	v_mfma_f32_16x16x32_bf16 v[84:87], v[202:205], v[186:189], v[84:87]
	v_mfma_f32_16x16x32_bf16 v[80:83], v[210:213], v[186:189], v[80:83]
	v_mfma_f32_16x16x32_bf16 v[68:71], v[202:205], v[194:197], v[68:71]
	v_mfma_f32_16x16x32_bf16 v[64:67], v[210:213], v[194:197], v[64:67]
	v_mfma_f32_16x16x32_bf16 v[116:119], v[206:209], v[174:177], v[116:119]
	v_mfma_f32_16x16x32_bf16 v[112:115], v[214:217], v[174:177], v[112:115]
	v_mfma_f32_16x16x32_bf16 v[100:103], v[206:209], v[182:185], v[100:103]
	v_mfma_f32_16x16x32_bf16 v[96:99], v[214:217], v[182:185], v[96:99]
	v_mfma_f32_16x16x32_bf16 v[84:87], v[206:209], v[190:193], v[84:87]
	v_mfma_f32_16x16x32_bf16 v[80:83], v[214:217], v[190:193], v[80:83]
	v_mfma_f32_16x16x32_bf16 v[68:71], v[206:209], v[198:201], v[68:71]
	v_mfma_f32_16x16x32_bf16 v[64:67], v[214:217], v[198:201], v[64:67]
	s_setprio 0
	s_mov_b32 m0, s52
	v_lshl_add_u64 v[218:219], v[222:223], 0, s[2:3]
	s_barrier
	ds_read_b128 v[170:173], v159 offset:49152
	ds_read_b128 v[174:177], v159 offset:50176
	ds_read_b128 v[178:181], v159 offset:51200
	ds_read_b128 v[182:185], v159 offset:52224
	ds_read_b128 v[186:189], v159 offset:53248
	ds_read_b128 v[190:193], v159 offset:54272
	ds_read_b128 v[194:197], v159 offset:55296
	ds_read_b128 v[198:201], v159 offset:56320
	global_load_lds_dwordx4 v[218:219], off
	v_lshl_add_u64 v[218:219], v[224:225], 0, s[2:3]
	s_mov_b32 m0, s53
	s_nop 0
	global_load_lds_dwordx4 v[218:219], off
	s_barrier
	s_waitcnt lgkmcnt(0)
	s_setprio 1
	s_waitcnt lgkmcnt(0)
	v_mfma_f32_16x16x32_bf16 v[60:63], v[148:151], v[170:173], v[60:63]
	v_mfma_f32_16x16x32_bf16 v[56:59], v[162:165], v[170:173], v[56:59]
	v_mfma_f32_16x16x32_bf16 v[44:47], v[148:151], v[178:181], v[44:47]
	v_mfma_f32_16x16x32_bf16 v[40:43], v[162:165], v[178:181], v[40:43]
	v_mfma_f32_16x16x32_bf16 v[28:31], v[148:151], v[186:189], v[28:31]
	v_mfma_f32_16x16x32_bf16 v[24:27], v[162:165], v[186:189], v[24:27]
	v_mfma_f32_16x16x32_bf16 v[12:15], v[148:151], v[194:197], v[12:15]
	v_mfma_f32_16x16x32_bf16 v[8:11], v[162:165], v[194:197], v[8:11]
	v_mfma_f32_16x16x32_bf16 v[60:63], v[152:155], v[174:177], v[60:63]
	v_mfma_f32_16x16x32_bf16 v[56:59], v[166:169], v[174:177], v[56:59]
	v_mfma_f32_16x16x32_bf16 v[44:47], v[152:155], v[182:185], v[44:47]
	v_mfma_f32_16x16x32_bf16 v[40:43], v[166:169], v[182:185], v[40:43]
	v_mfma_f32_16x16x32_bf16 v[28:31], v[152:155], v[190:193], v[28:31]
	v_mfma_f32_16x16x32_bf16 v[24:27], v[166:169], v[190:193], v[24:27]
	v_mfma_f32_16x16x32_bf16 v[12:15], v[152:155], v[198:201], v[12:15]
	v_mfma_f32_16x16x32_bf16 v[8:11], v[166:169], v[198:201], v[8:11]
	s_setprio 0
	s_barrier
	s_add_u32 s10, s10, 0x40080
	s_addc_u32 s11, s11, 0
	s_add_i32 s12, s12, s45
	v_lshl_add_u64 v[148:149], s[10:11], 0, v[128:129]
	s_mov_b32 m0, s12
	s_nop 0
	global_load_lds_dwordx4 v[148:149], off
	v_lshl_add_u64 v[148:149], s[10:11], 0, v[130:131]
	s_add_i32 m0, s12, 0x2000
	s_nop 0
	global_load_lds_dwordx4 v[148:149], off
	s_waitcnt vmcnt(6)
	s_barrier
	s_setprio 1
	v_mfma_f32_16x16x32_bf16 v[52:55], v[202:205], v[170:173], v[52:55]
	v_mfma_f32_16x16x32_bf16 v[48:51], v[210:213], v[170:173], v[48:51]
	v_mfma_f32_16x16x32_bf16 v[36:39], v[202:205], v[178:181], v[36:39]
	v_mfma_f32_16x16x32_bf16 v[32:35], v[210:213], v[178:181], v[32:35]
	v_mfma_f32_16x16x32_bf16 v[20:23], v[202:205], v[186:189], v[20:23]
	v_mfma_f32_16x16x32_bf16 v[16:19], v[210:213], v[186:189], v[16:19]
	v_mfma_f32_16x16x32_bf16 v[4:7], v[202:205], v[194:197], v[4:7]
	v_mfma_f32_16x16x32_bf16 v[0:3], v[210:213], v[194:197], v[0:3]
	v_mfma_f32_16x16x32_bf16 v[52:55], v[206:209], v[174:177], v[52:55]
	v_mfma_f32_16x16x32_bf16 v[48:51], v[214:217], v[174:177], v[48:51]
	v_mfma_f32_16x16x32_bf16 v[36:39], v[206:209], v[182:185], v[36:39]
	v_mfma_f32_16x16x32_bf16 v[32:35], v[214:217], v[182:185], v[32:35]
	v_mfma_f32_16x16x32_bf16 v[20:23], v[206:209], v[190:193], v[20:23]
	v_mfma_f32_16x16x32_bf16 v[16:19], v[214:217], v[190:193], v[16:19]
	v_mfma_f32_16x16x32_bf16 v[4:7], v[206:209], v[198:201], v[4:7]
	v_mfma_f32_16x16x32_bf16 v[0:3], v[214:217], v[198:201], v[0:3]
	s_setprio 0
	s_add_i32 s23, s23, 2
	s_add_u32 s8, s8, 0x100
	s_addc_u32 s9, s9, 0
	s_add_u32 s17, s17, 0x100
	s_addc_u32 s21, s21, 0
	s_cmp_gt_u32 s23, 13
	s_barrier
	s_cbranch_scc0 .LBB0_1076
	v_lshl_add_u32 v161, s0, 8, v156
	s_lshl_b32 s0, s28, 8
	s_or_b32 s38, s0, s51
	v_lshlrev_b32_e32 v152, 4, v161
	v_lshlrev_b32_e32 v216, 6, v161
	v_mov_b32_e32 v217, 0
	v_lshl_add_u64 v[216:217], v[216:217], 0, v[138:139]
	v_lshlrev_b32_e32 v248, 6, v161
	v_add_u32_e32 v248, 0x2000, v248
	v_mov_b32_e32 v249, 0
	v_lshl_add_u64 v[248:249], v[248:249], 0, v[138:139]
	global_load_dwordx4 v[172:175], v[216:217], off offset:0
	global_load_dwordx4 v[176:179], v[216:217], off offset:32
	global_load_dwordx4 v[180:183], v[216:217], off offset:1024
	global_load_dwordx4 v[184:187], v[216:217], off offset:1056
	global_load_dwordx4 v[188:191], v[216:217], off offset:2048
	global_load_dwordx4 v[192:195], v[216:217], off offset:2080
	global_load_dwordx4 v[196:199], v[216:217], off offset:3072
	global_load_dwordx4 v[200:203], v[216:217], off offset:3104
	global_load_dwordx4 v[204:207], v[248:249], off offset:0
	global_load_dwordx4 v[208:211], v[248:249], off offset:32
	global_load_dwordx4 v[212:215], v[248:249], off offset:1024
	global_load_dwordx4 v[228:231], v[248:249], off offset:1056
	global_load_dwordx4 v[232:235], v[248:249], off offset:2048
	global_load_dwordx4 v[236:239], v[248:249], off offset:2080
	global_load_dwordx4 v[240:243], v[248:249], off offset:3072
	global_load_dwordx4 v[244:247], v[248:249], off offset:3104
	s_waitcnt vmcnt(0)
	v_or_b32_e32 v148, s38, v134
	v_cndmask_b32_e64 v132, 0, 1, s[18:19]
	v_ashrrev_i32_e32 v153, 31, v152
	v_cmp_ne_u32_e64 s[8:9], 1, v132
	s_andn2_b64 vcc, exec, s[18:19]
	v_cmp_lt_i32_e64 s[0:1], s57, v148
	s_cbranch_vccnz .LBB0_1087
	s_mov_b64 s[12:13], -1
	s_and_saveexec_b64 s[10:11], s[0:1]
	s_cbranch_execz .LBB0_1084
	s_cmp_lt_i32 s28, 8
	s_cbranch_scc1 .LBB0_1081
	s_cmp_eq_u32 s28, 8
	s_cselect_b64 s[0:1], -1, 0
	s_cbranch_execz .LBB0_1082
	s_branch .LBB0_1083

.LBB0_1084:
	s_or_b64 exec, exec, s[10:11]
	s_and_saveexec_b64 s[0:1], s[12:13]
	s_cbranch_execz .LBB0_1086
	v_lshl_add_u64 v[150:151], v[152:153], 2, v[138:139]
	v_mov_b32_e32 v154, v126
	v_mov_b32_e32 v155, v126
	v_mov_b32_e32 v150, v125
	v_mov_b32_e32 v151, v125
	s_nop 1
	v_permlane32_swap_b32 v155, v154
	v_mov_b32_e32 v132, v124
	v_mov_b32_e32 v149, v124
	s_nop 1
	v_permlane32_swap_b32 v150, v151
	v_cndmask_b32_e64 v154, v154, v155, s[4:5]
	v_mov_b32_e32 v155, v127
	v_mov_b32_e32 v170, v127
	s_nop 1
	v_permlane32_swap_b32 v132, v149
	s_nop 1
	v_permlane32_swap_b32 v155, v170
	v_cndmask_b32_e64 v151, v151, v150, s[4:5]
	v_cndmask_b32_e64 v150, v149, v132, s[4:5]
	v_cndmask_b32_e64 v155, v170, v155, s[4:5]
	v_pk_mul_f32 v[150:151], v[136:137], v[150:151]
	v_mul_f32_e32 v132, v136, v154
	v_mov_b32_e32 v162, v172
	v_mov_b32_e32 v163, v173
	v_mov_b32_e32 v164, v174
	v_mov_b32_e32 v165, v175
	v_mov_b32_e32 v166, v176
	v_mov_b32_e32 v167, v177
	v_mov_b32_e32 v168, v178
	v_mov_b32_e32 v169, v179
	v_mul_f32_e32 v126, v126, v164
	v_pk_mul_f32 v[150:151], v[166:167], v[150:151]
	v_mul_f32_e32 v154, v168, v132
	v_mul_f32_e32 v167, v136, v155
	v_mov_b32_e32 v166, v127
	v_mov_b32_e32 v168, v165
	v_pk_mul_f32 v[164:165], v[166:167], v[168:169]
	v_pk_fma_f32 v[124:125], v[124:125], v[162:163], v[150:151]
	v_mov_b32_e32 v127, v164
	v_mov_b32_e32 v155, v165
	v_pk_add_f32 v[126:127], v[126:127], v[154:155]

.LBB0_1104:
	s_or_b64 exec, exec, s[12:13]
	s_and_saveexec_b64 s[0:1], s[16:17]
	s_cbranch_execz .LBB0_1106
	v_lshl_add_u64 v[126:127], v[152:153], 2, v[138:139]
	v_mov_b32_e32 v152, v118
	v_mov_b32_e32 v153, v118
	s_nop 1
	v_permlane32_swap_b32 v153, v152
	v_mov_b32_e32 v121, v116
	v_mov_b32_e32 v126, v116
	v_cndmask_b32_e64 v152, v152, v153, s[4:5]
	v_mov_b32_e32 v153, v119
	v_mov_b32_e32 v166, v119
	s_nop 1
	v_permlane32_swap_b32 v121, v126
	v_mov_b32_e32 v127, v117
	v_mov_b32_e32 v132, v117
	s_nop 1
	v_permlane32_swap_b32 v153, v166
	s_nop 1
	v_permlane32_swap_b32 v132, v127
	v_cndmask_b32_e64 v126, v126, v121, s[4:5]
	v_cndmask_b32_e64 v153, v166, v153, s[4:5]
	v_mul_f32_e32 v121, v136, v152
	v_cndmask_b32_e64 v127, v127, v132, s[4:5]
	v_mul_f32_e32 v153, v136, v153
	v_mov_b32_e32 v152, v119
	v_pk_mul_f32 v[126:127], v[136:137], v[126:127]
	v_mov_b32_e32 v122, v172
	v_mov_b32_e32 v123, v173
	v_mov_b32_e32 v124, v174
	v_mov_b32_e32 v125, v175
	v_mov_b32_e32 v162, v176
	v_mov_b32_e32 v163, v177
	v_mov_b32_e32 v164, v178
	v_mov_b32_e32 v165, v179
	v_mul_f32_e32 v118, v118, v124
	v_mul_f32_e32 v124, v164, v121
	v_mov_b32_e32 v164, v125
	v_pk_mul_f32 v[152:153], v[152:153], v[164:165]
	v_pk_mul_f32 v[126:127], v[162:163], v[126:127]
	v_mov_b32_e32 v119, v152
	v_mov_b32_e32 v125, v153
	v_pk_fma_f32 v[116:117], v[116:117], v[122:123], v[126:127]
	v_pk_add_f32 v[118:119], v[118:119], v[124:125]

.LBB0_1124:
	s_or_b64 exec, exec, s[0:1]
	s_and_saveexec_b64 s[0:1], s[40:41]
	s_cbranch_execz .LBB0_1126
	v_lshl_add_u64 v[112:113], v[114:115], 2, v[138:139]
	v_mov_b32_e32 v119, v110
	v_mov_b32_e32 v121, v110
	s_nop 1
	v_permlane32_swap_b32 v119, v121
	v_mov_b32_e32 v112, v108
	v_mov_b32_e32 v117, v108
	v_cndmask_b32_e64 v119, v121, v119, s[4:5]
	v_mov_b32_e32 v121, v111
	v_mov_b32_e32 v126, v111
	s_nop 1
	v_permlane32_swap_b32 v112, v117
	v_mov_b32_e32 v113, v109
	v_mov_b32_e32 v118, v109
	s_nop 1
	v_permlane32_swap_b32 v121, v126
	s_nop 1
	v_permlane32_swap_b32 v118, v113
	v_cndmask_b32_e64 v112, v117, v112, s[4:5]
	v_cndmask_b32_e64 v121, v126, v121, s[4:5]
	v_mul_f32_e32 v117, v136, v119
	v_cndmask_b32_e64 v113, v113, v118, s[4:5]
	v_mul_f32_e32 v127, v136, v121
	v_mov_b32_e32 v126, v111
	v_pk_mul_f32 v[112:113], v[136:137], v[112:113]
	v_mov_b32_e32 v122, v180
	v_mov_b32_e32 v123, v181
	v_mov_b32_e32 v124, v182
	v_mov_b32_e32 v125, v183
	v_mov_b32_e32 v150, v184
	v_mov_b32_e32 v151, v185
	v_mov_b32_e32 v152, v186
	v_mov_b32_e32 v153, v187
	v_mul_f32_e32 v110, v110, v124
	v_mul_f32_e32 v118, v152, v117
	v_mov_b32_e32 v152, v125
	v_pk_mul_f32 v[124:125], v[126:127], v[152:153]
	v_pk_mul_f32 v[112:113], v[150:151], v[112:113]
	v_mov_b32_e32 v111, v124
	v_mov_b32_e32 v119, v125
	v_pk_fma_f32 v[108:109], v[108:109], v[122:123], v[112:113]
	v_pk_add_f32 v[110:111], v[110:111], v[118:119]

.LBB0_1145:
	s_or_b64 exec, exec, s[0:1]
	s_and_saveexec_b64 s[0:1], s[40:41]
	s_cbranch_execz .LBB0_1147
	v_lshl_add_u64 v[108:109], v[114:115], 2, v[138:139]
	s_nop 0
	v_mov_b32_e32 v121, v102
	v_mov_b32_e32 v122, v102
	v_mov_b32_e32 v114, v100
	v_mov_b32_e32 v118, v100
	v_mov_b32_e32 v115, v101
	v_mov_b32_e32 v119, v101
	s_nop 1
	v_permlane32_swap_b32 v121, v122
	s_nop 1
	v_permlane32_swap_b32 v118, v114
	s_nop 1
	v_permlane32_swap_b32 v119, v115
	v_mov_b32_e32 v123, v103
	v_cndmask_b32_e64 v121, v122, v121, s[4:5]
	v_mov_b32_e32 v122, v103
	s_nop 1
	v_permlane32_swap_b32 v122, v123
	v_cndmask_b32_e64 v115, v115, v119, s[4:5]
	v_cndmask_b32_e64 v114, v114, v118, s[4:5]
	v_cndmask_b32_e64 v122, v123, v122, s[4:5]
	v_pk_mul_f32 v[114:115], v[136:137], v[114:115]
	v_mov_b32_e32 v104, v180
	v_mov_b32_e32 v105, v181
	v_mov_b32_e32 v106, v182
	v_mov_b32_e32 v107, v183
	v_mov_b32_e32 v108, v184
	v_mov_b32_e32 v109, v185
	v_mov_b32_e32 v110, v186
	v_mov_b32_e32 v111, v187
	v_mul_f32_e32 v102, v102, v106
	v_mul_f32_e32 v106, v136, v121
	v_pk_mul_f32 v[108:109], v[108:109], v[114:115]
	v_mul_f32_e32 v106, v110, v106
	v_mul_f32_e32 v115, v136, v122
	v_mov_b32_e32 v114, v103
	v_mov_b32_e32 v110, v107
	v_pk_mul_f32 v[110:111], v[114:115], v[110:111]
	v_pk_fma_f32 v[100:101], v[100:101], v[104:105], v[108:109]
	v_mov_b32_e32 v103, v110
	v_mov_b32_e32 v107, v111
	v_pk_add_f32 v[102:103], v[102:103], v[106:107]

.LBB0_1164:
	s_or_b64 exec, exec, s[0:1]
	s_and_saveexec_b64 s[0:1], s[40:41]
	s_cbranch_execz .LBB0_1166
	v_lshl_add_u64 v[96:97], v[98:99], 2, v[138:139]
	v_mov_b32_e32 v111, v94
	v_mov_b32_e32 v112, v94
	v_mov_b32_e32 v96, v92
	v_mov_b32_e32 v101, v92
	v_mov_b32_e32 v97, v93
	v_mov_b32_e32 v110, v93
	s_nop 1
	v_permlane32_swap_b32 v112, v111
	s_nop 1
	v_permlane32_swap_b32 v101, v96
	s_nop 1
	v_permlane32_swap_b32 v97, v110
	v_mov_b32_e32 v113, v95
	v_cndmask_b32_e64 v111, v111, v112, s[4:5]
	v_mov_b32_e32 v112, v95
	s_nop 1
	v_permlane32_swap_b32 v113, v112
	v_cndmask_b32_e64 v97, v110, v97, s[4:5]
	v_cndmask_b32_e64 v96, v96, v101, s[4:5]
	v_cndmask_b32_e64 v112, v112, v113, s[4:5]
	v_pk_mul_f32 v[96:97], v[136:137], v[96:97]
	v_mul_f32_e32 v101, v136, v111
	v_mov_b32_e32 v102, v188
	v_mov_b32_e32 v103, v189
	v_mov_b32_e32 v104, v190
	v_mov_b32_e32 v105, v191
	v_mov_b32_e32 v106, v192
	v_mov_b32_e32 v107, v193
	v_mov_b32_e32 v108, v194
	v_mov_b32_e32 v109, v195
	v_mul_f32_e32 v94, v94, v104
	v_pk_mul_f32 v[96:97], v[106:107], v[96:97]
	v_mul_f32_e32 v104, v108, v101
	v_mul_f32_e32 v107, v136, v112
	v_mov_b32_e32 v106, v95
	v_mov_b32_e32 v108, v105
	v_pk_mul_f32 v[106:107], v[106:107], v[108:109]
	v_pk_fma_f32 v[92:93], v[92:93], v[102:103], v[96:97]
	v_mov_b32_e32 v95, v106
	v_mov_b32_e32 v105, v107
	v_pk_add_f32 v[94:95], v[94:95], v[104:105]

.LBB0_1185:
	s_or_b64 exec, exec, s[0:1]
	s_and_saveexec_b64 s[0:1], s[40:41]
	s_cbranch_execz .LBB0_1187
	v_lshl_add_u64 v[92:93], v[98:99], 2, v[138:139]
	s_nop 0
	v_mov_b32_e32 v104, v86
	v_mov_b32_e32 v105, v86
	v_mov_b32_e32 v98, v84
	v_mov_b32_e32 v102, v84
	v_mov_b32_e32 v99, v85
	v_mov_b32_e32 v103, v85
	s_nop 1
	v_permlane32_swap_b32 v105, v104
	s_nop 1
	v_permlane32_swap_b32 v102, v98
	s_nop 1
	v_permlane32_swap_b32 v99, v103
	v_mov_b32_e32 v106, v87
	v_cndmask_b32_e64 v104, v104, v105, s[4:5]
	v_mov_b32_e32 v105, v87
	s_nop 1
	v_permlane32_swap_b32 v106, v105
	v_cndmask_b32_e64 v99, v103, v99, s[4:5]
	v_cndmask_b32_e64 v98, v98, v102, s[4:5]
	v_cndmask_b32_e64 v105, v105, v106, s[4:5]
	v_pk_mul_f32 v[98:99], v[136:137], v[98:99]
	v_mov_b32_e32 v88, v188
	v_mov_b32_e32 v89, v189
	v_mov_b32_e32 v90, v190
	v_mov_b32_e32 v91, v191
	v_mov_b32_e32 v92, v192
	v_mov_b32_e32 v93, v193
	v_mov_b32_e32 v94, v194
	v_mov_b32_e32 v95, v195
	v_mul_f32_e32 v86, v86, v90
	v_mul_f32_e32 v90, v136, v104
	v_pk_mul_f32 v[92:93], v[92:93], v[98:99]
	v_mul_f32_e32 v90, v94, v90
	v_mul_f32_e32 v99, v136, v105
	v_mov_b32_e32 v98, v87
	v_mov_b32_e32 v94, v91
	v_pk_mul_f32 v[94:95], v[98:99], v[94:95]
	v_pk_fma_f32 v[84:85], v[84:85], v[88:89], v[92:93]
	v_mov_b32_e32 v87, v94
	v_mov_b32_e32 v91, v95
	v_pk_add_f32 v[86:87], v[86:87], v[90:91]

.LBB0_1204:
	s_or_b64 exec, exec, s[0:1]
	s_and_saveexec_b64 s[0:1], s[40:41]
	s_cbranch_execz .LBB0_1206
	v_lshl_add_u64 v[80:81], v[82:83], 2, v[138:139]
	v_mov_b32_e32 v95, v78
	v_mov_b32_e32 v96, v78
	v_mov_b32_e32 v80, v76
	v_mov_b32_e32 v85, v76
	v_mov_b32_e32 v81, v77
	v_mov_b32_e32 v94, v77
	s_nop 1
	v_permlane32_swap_b32 v96, v95
	s_nop 1
	v_permlane32_swap_b32 v80, v85
	s_nop 1
	v_permlane32_swap_b32 v94, v81
	v_mov_b32_e32 v97, v79
	v_cndmask_b32_e64 v95, v95, v96, s[4:5]
	v_mov_b32_e32 v96, v79
	s_nop 1
	v_permlane32_swap_b32 v96, v97
	v_cndmask_b32_e64 v81, v81, v94, s[4:5]
	v_cndmask_b32_e64 v80, v85, v80, s[4:5]
	v_cndmask_b32_e64 v96, v97, v96, s[4:5]
	v_pk_mul_f32 v[80:81], v[136:137], v[80:81]
	v_mul_f32_e32 v85, v136, v95
	v_mov_b32_e32 v86, v196
	v_mov_b32_e32 v87, v197
	v_mov_b32_e32 v88, v198
	v_mov_b32_e32 v89, v199
	v_mov_b32_e32 v90, v200
	v_mov_b32_e32 v91, v201
	v_mov_b32_e32 v92, v202
	v_mov_b32_e32 v93, v203
	v_mul_f32_e32 v78, v78, v88
	v_pk_mul_f32 v[80:81], v[90:91], v[80:81]
	v_mul_f32_e32 v88, v92, v85
	v_mul_f32_e32 v91, v136, v96
	v_mov_b32_e32 v90, v79
	v_mov_b32_e32 v92, v89
	v_pk_mul_f32 v[90:91], v[90:91], v[92:93]
	v_pk_fma_f32 v[76:77], v[76:77], v[86:87], v[80:81]
	v_mov_b32_e32 v79, v90
	v_mov_b32_e32 v89, v91
	v_pk_add_f32 v[78:79], v[78:79], v[88:89]

.LBB0_1225:
	s_or_b64 exec, exec, s[0:1]
	s_and_saveexec_b64 s[0:1], s[40:41]
	s_cbranch_execz .LBB0_1227
	v_lshl_add_u64 v[76:77], v[82:83], 2, v[138:139]
	s_nop 0
	v_mov_b32_e32 v88, v70
	v_mov_b32_e32 v89, v70
	v_mov_b32_e32 v82, v68
	v_mov_b32_e32 v86, v68
	v_mov_b32_e32 v83, v69
	v_mov_b32_e32 v87, v69
	s_nop 1
	v_permlane32_swap_b32 v89, v88
	s_nop 1
	v_permlane32_swap_b32 v82, v86
	s_nop 1
	v_permlane32_swap_b32 v87, v83
	v_mov_b32_e32 v90, v71
	v_cndmask_b32_e64 v88, v88, v89, s[4:5]
	v_mov_b32_e32 v89, v71
	s_nop 1
	v_permlane32_swap_b32 v89, v90
	v_cndmask_b32_e64 v83, v83, v87, s[4:5]
	v_cndmask_b32_e64 v82, v86, v82, s[4:5]
	v_cndmask_b32_e64 v89, v90, v89, s[4:5]
	v_pk_mul_f32 v[82:83], v[136:137], v[82:83]
	v_mov_b32_e32 v72, v196
	v_mov_b32_e32 v73, v197
	v_mov_b32_e32 v74, v198
	v_mov_b32_e32 v75, v199
	v_mov_b32_e32 v76, v200
	v_mov_b32_e32 v77, v201
	v_mov_b32_e32 v78, v202
	v_mov_b32_e32 v79, v203
	v_mul_f32_e32 v70, v70, v74
	v_mul_f32_e32 v74, v136, v88
	v_pk_mul_f32 v[76:77], v[76:77], v[82:83]
	v_mul_f32_e32 v74, v78, v74
	v_mul_f32_e32 v83, v136, v89
	v_mov_b32_e32 v82, v71
	v_mov_b32_e32 v78, v75
	v_pk_mul_f32 v[78:79], v[82:83], v[78:79]
	v_pk_fma_f32 v[68:69], v[68:69], v[72:73], v[76:77]
	v_mov_b32_e32 v71, v78
	v_mov_b32_e32 v75, v79
	v_pk_add_f32 v[70:71], v[70:71], v[74:75]

.LBB0_1244:
	s_or_b64 exec, exec, s[0:1]
	s_and_saveexec_b64 s[0:1], s[40:41]
	s_cbranch_execz .LBB0_1246
	v_lshl_add_u64 v[64:65], v[66:67], 2, v[138:139]
	v_mov_b32_e32 v79, v62
	v_mov_b32_e32 v80, v62
	v_mov_b32_e32 v64, v60
	v_mov_b32_e32 v69, v60
	v_mov_b32_e32 v65, v61
	v_mov_b32_e32 v78, v61
	s_nop 1
	v_permlane32_swap_b32 v79, v80
	s_nop 1
	v_permlane32_swap_b32 v69, v64
	s_nop 1
	v_permlane32_swap_b32 v78, v65
	v_mov_b32_e32 v81, v63
	v_cndmask_b32_e64 v79, v80, v79, s[4:5]
	v_mov_b32_e32 v80, v63
	s_nop 1
	v_permlane32_swap_b32 v81, v80
	v_cndmask_b32_e64 v65, v65, v78, s[4:5]
	v_cndmask_b32_e64 v64, v64, v69, s[4:5]
	v_cndmask_b32_e64 v80, v80, v81, s[4:5]
	v_pk_mul_f32 v[64:65], v[136:137], v[64:65]
	v_mul_f32_e32 v69, v136, v79
	v_mov_b32_e32 v70, v204
	v_mov_b32_e32 v71, v205
	v_mov_b32_e32 v72, v206
	v_mov_b32_e32 v73, v207
	v_mov_b32_e32 v74, v208
	v_mov_b32_e32 v75, v209
	v_mov_b32_e32 v76, v210
	v_mov_b32_e32 v77, v211
	v_mul_f32_e32 v62, v62, v72
	v_pk_mul_f32 v[64:65], v[74:75], v[64:65]
	v_mul_f32_e32 v72, v76, v69
	v_mul_f32_e32 v75, v136, v80
	v_mov_b32_e32 v74, v63
	v_mov_b32_e32 v76, v73
	v_pk_mul_f32 v[74:75], v[74:75], v[76:77]
	v_pk_fma_f32 v[60:61], v[60:61], v[70:71], v[64:65]
	v_mov_b32_e32 v63, v74
	v_mov_b32_e32 v73, v75
	v_pk_add_f32 v[62:63], v[62:63], v[72:73]

.LBB0_1265:
	s_or_b64 exec, exec, s[0:1]
	s_and_saveexec_b64 s[0:1], s[40:41]
	s_cbranch_execz .LBB0_1267
	v_lshl_add_u64 v[60:61], v[66:67], 2, v[138:139]
	s_nop 0
	v_mov_b32_e32 v72, v54
	v_mov_b32_e32 v73, v54
	v_mov_b32_e32 v66, v52
	v_mov_b32_e32 v70, v52
	v_mov_b32_e32 v67, v53
	v_mov_b32_e32 v71, v53
	s_nop 1
	v_permlane32_swap_b32 v72, v73
	s_nop 1
	v_permlane32_swap_b32 v70, v66
	s_nop 1
	v_permlane32_swap_b32 v71, v67
	v_mov_b32_e32 v74, v55
	v_cndmask_b32_e64 v72, v73, v72, s[4:5]
	v_mov_b32_e32 v73, v55
	s_nop 1
	v_permlane32_swap_b32 v74, v73
	v_cndmask_b32_e64 v67, v67, v71, s[4:5]
	v_cndmask_b32_e64 v66, v66, v70, s[4:5]
	v_cndmask_b32_e64 v73, v73, v74, s[4:5]
	v_pk_mul_f32 v[66:67], v[136:137], v[66:67]
	v_mov_b32_e32 v56, v204
	v_mov_b32_e32 v57, v205
	v_mov_b32_e32 v58, v206
	v_mov_b32_e32 v59, v207
	v_mov_b32_e32 v60, v208
	v_mov_b32_e32 v61, v209
	v_mov_b32_e32 v62, v210
	v_mov_b32_e32 v63, v211
	v_mul_f32_e32 v54, v54, v58
	v_mul_f32_e32 v58, v136, v72
	v_pk_mul_f32 v[60:61], v[60:61], v[66:67]
	v_mul_f32_e32 v58, v62, v58
	v_mul_f32_e32 v67, v136, v73
	v_mov_b32_e32 v66, v55
	v_mov_b32_e32 v62, v59
	v_pk_mul_f32 v[62:63], v[66:67], v[62:63]
	v_pk_fma_f32 v[52:53], v[52:53], v[56:57], v[60:61]
	v_mov_b32_e32 v55, v62
	v_mov_b32_e32 v59, v63
	v_pk_add_f32 v[54:55], v[54:55], v[58:59]

.LBB0_1284:
	s_or_b64 exec, exec, s[0:1]
	s_and_saveexec_b64 s[0:1], s[40:41]
	s_cbranch_execz .LBB0_1286
	v_lshl_add_u64 v[48:49], v[50:51], 2, v[138:139]
	v_mov_b32_e32 v63, v46
	v_mov_b32_e32 v64, v46
	v_mov_b32_e32 v48, v44
	v_mov_b32_e32 v53, v44
	v_mov_b32_e32 v49, v45
	v_mov_b32_e32 v62, v45
	s_nop 1
	v_permlane32_swap_b32 v64, v63
	s_nop 1
	v_permlane32_swap_b32 v53, v48
	s_nop 1
	v_permlane32_swap_b32 v49, v62
	v_mov_b32_e32 v65, v47
	v_cndmask_b32_e64 v63, v63, v64, s[4:5]
	v_mov_b32_e32 v64, v47
	s_nop 1
	v_permlane32_swap_b32 v65, v64
	v_cndmask_b32_e64 v49, v62, v49, s[4:5]
	v_cndmask_b32_e64 v48, v48, v53, s[4:5]
	v_cndmask_b32_e64 v64, v64, v65, s[4:5]
	v_pk_mul_f32 v[48:49], v[136:137], v[48:49]
	v_mul_f32_e32 v53, v136, v63
	v_mov_b32_e32 v54, v212
	v_mov_b32_e32 v55, v213
	v_mov_b32_e32 v56, v214
	v_mov_b32_e32 v57, v215
	v_mov_b32_e32 v58, v228
	v_mov_b32_e32 v59, v229
	v_mov_b32_e32 v60, v230
	v_mov_b32_e32 v61, v231
	v_mul_f32_e32 v46, v46, v56
	v_pk_mul_f32 v[48:49], v[58:59], v[48:49]
	v_mul_f32_e32 v56, v60, v53
	v_mul_f32_e32 v59, v136, v64
	v_mov_b32_e32 v58, v47
	v_mov_b32_e32 v60, v57
	v_pk_mul_f32 v[58:59], v[58:59], v[60:61]
	v_pk_fma_f32 v[44:45], v[44:45], v[54:55], v[48:49]
	v_mov_b32_e32 v47, v58
	v_mov_b32_e32 v57, v59
	v_pk_add_f32 v[46:47], v[46:47], v[56:57]

.LBB0_1305:
	s_or_b64 exec, exec, s[0:1]
	s_and_saveexec_b64 s[0:1], s[40:41]
	s_cbranch_execz .LBB0_1307
	v_lshl_add_u64 v[44:45], v[50:51], 2, v[138:139]
	s_nop 0
	v_mov_b32_e32 v56, v38
	v_mov_b32_e32 v57, v38
	v_mov_b32_e32 v50, v36
	v_mov_b32_e32 v54, v36
	v_mov_b32_e32 v51, v37
	v_mov_b32_e32 v55, v37
	s_nop 1
	v_permlane32_swap_b32 v57, v56
	s_nop 1
	v_permlane32_swap_b32 v50, v54
	s_nop 1
	v_permlane32_swap_b32 v51, v55
	v_mov_b32_e32 v58, v39
	v_cndmask_b32_e64 v56, v56, v57, s[4:5]
	v_mov_b32_e32 v57, v39
	s_nop 1
	v_permlane32_swap_b32 v58, v57
	v_cndmask_b32_e64 v51, v55, v51, s[4:5]
	v_cndmask_b32_e64 v50, v54, v50, s[4:5]
	v_cndmask_b32_e64 v57, v57, v58, s[4:5]
	v_pk_mul_f32 v[50:51], v[136:137], v[50:51]
	v_mov_b32_e32 v40, v212
	v_mov_b32_e32 v41, v213
	v_mov_b32_e32 v42, v214
	v_mov_b32_e32 v43, v215
	v_mov_b32_e32 v44, v228
	v_mov_b32_e32 v45, v229
	v_mov_b32_e32 v46, v230
	v_mov_b32_e32 v47, v231
	v_mul_f32_e32 v38, v38, v42
	v_mul_f32_e32 v42, v136, v56
	v_pk_mul_f32 v[44:45], v[44:45], v[50:51]
	v_mul_f32_e32 v42, v46, v42
	v_mul_f32_e32 v51, v136, v57
	v_mov_b32_e32 v50, v39
	v_mov_b32_e32 v46, v43
	v_pk_mul_f32 v[46:47], v[50:51], v[46:47]
	v_pk_fma_f32 v[36:37], v[36:37], v[40:41], v[44:45]
	v_mov_b32_e32 v39, v46
	v_mov_b32_e32 v43, v47
	v_pk_add_f32 v[38:39], v[38:39], v[42:43]

.LBB0_1324:
	s_or_b64 exec, exec, s[0:1]
	s_and_saveexec_b64 s[0:1], s[40:41]
	s_cbranch_execz .LBB0_1326
	v_lshl_add_u64 v[32:33], v[34:35], 2, v[138:139]
	v_mov_b32_e32 v47, v30
	v_mov_b32_e32 v48, v30
	v_mov_b32_e32 v32, v28
	v_mov_b32_e32 v37, v28
	v_mov_b32_e32 v33, v29
	v_mov_b32_e32 v46, v29
	s_nop 1
	v_permlane32_swap_b32 v48, v47
	s_nop 1
	v_permlane32_swap_b32 v32, v37
	s_nop 1
	v_permlane32_swap_b32 v46, v33
	v_mov_b32_e32 v49, v31
	v_cndmask_b32_e64 v47, v47, v48, s[4:5]
	v_mov_b32_e32 v48, v31
	s_nop 1
	v_permlane32_swap_b32 v48, v49
	v_cndmask_b32_e64 v33, v33, v46, s[4:5]
	v_cndmask_b32_e64 v32, v37, v32, s[4:5]
	v_cndmask_b32_e64 v48, v49, v48, s[4:5]
	v_pk_mul_f32 v[32:33], v[136:137], v[32:33]
	v_mul_f32_e32 v37, v136, v47
	v_mov_b32_e32 v38, v232
	v_mov_b32_e32 v39, v233
	v_mov_b32_e32 v40, v234
	v_mov_b32_e32 v41, v235
	v_mov_b32_e32 v42, v236
	v_mov_b32_e32 v43, v237
	v_mov_b32_e32 v44, v238
	v_mov_b32_e32 v45, v239
	v_mul_f32_e32 v30, v30, v40
	v_pk_mul_f32 v[32:33], v[42:43], v[32:33]
	v_mul_f32_e32 v40, v44, v37
	v_mul_f32_e32 v43, v136, v48
	v_mov_b32_e32 v42, v31
	v_mov_b32_e32 v44, v41
	v_pk_mul_f32 v[42:43], v[42:43], v[44:45]
	v_pk_fma_f32 v[28:29], v[28:29], v[38:39], v[32:33]
	v_mov_b32_e32 v31, v42
	v_mov_b32_e32 v41, v43
	v_pk_add_f32 v[30:31], v[30:31], v[40:41]

.LBB0_1345:
	s_or_b64 exec, exec, s[0:1]
	s_and_saveexec_b64 s[0:1], s[40:41]
	s_cbranch_execz .LBB0_1347
	v_lshl_add_u64 v[28:29], v[34:35], 2, v[138:139]
	s_nop 0
	v_mov_b32_e32 v40, v22
	v_mov_b32_e32 v41, v22
	v_mov_b32_e32 v34, v20
	v_mov_b32_e32 v38, v20
	v_mov_b32_e32 v35, v21
	v_mov_b32_e32 v39, v21
	s_nop 1
	v_permlane32_swap_b32 v40, v41
	s_nop 1
	v_permlane32_swap_b32 v38, v34
	s_nop 1
	v_permlane32_swap_b32 v39, v35
	v_mov_b32_e32 v42, v23
	v_cndmask_b32_e64 v40, v41, v40, s[4:5]
	v_mov_b32_e32 v41, v23
	s_nop 1
	v_permlane32_swap_b32 v41, v42
	v_cndmask_b32_e64 v35, v35, v39, s[4:5]
	v_cndmask_b32_e64 v34, v34, v38, s[4:5]
	v_cndmask_b32_e64 v41, v42, v41, s[4:5]
	v_pk_mul_f32 v[34:35], v[136:137], v[34:35]
	v_mov_b32_e32 v24, v232
	v_mov_b32_e32 v25, v233
	v_mov_b32_e32 v26, v234
	v_mov_b32_e32 v27, v235
	v_mov_b32_e32 v28, v236
	v_mov_b32_e32 v29, v237
	v_mov_b32_e32 v30, v238
	v_mov_b32_e32 v31, v239
	v_mul_f32_e32 v22, v22, v26
	v_mul_f32_e32 v26, v136, v40
	v_pk_mul_f32 v[28:29], v[28:29], v[34:35]
	v_mul_f32_e32 v26, v30, v26
	v_mul_f32_e32 v35, v136, v41
	v_mov_b32_e32 v34, v23
	v_mov_b32_e32 v30, v27
	v_pk_mul_f32 v[30:31], v[34:35], v[30:31]
	v_pk_fma_f32 v[20:21], v[20:21], v[24:25], v[28:29]
	v_mov_b32_e32 v23, v30
	v_mov_b32_e32 v27, v31
	v_pk_add_f32 v[22:23], v[22:23], v[26:27]

.LBB0_1364:
	s_or_b64 exec, exec, s[0:1]
	s_and_saveexec_b64 s[0:1], s[40:41]
	s_cbranch_execz .LBB0_1366
	v_lshl_add_u64 v[16:17], v[18:19], 2, v[138:139]
	v_mov_b32_e32 v31, v14
	v_mov_b32_e32 v32, v14
	v_mov_b32_e32 v16, v12
	v_mov_b32_e32 v21, v12
	v_mov_b32_e32 v17, v13
	v_mov_b32_e32 v30, v13
	s_nop 1
	v_permlane32_swap_b32 v31, v32
	s_nop 1
	v_permlane32_swap_b32 v21, v16
	s_nop 1
	v_permlane32_swap_b32 v17, v30
	v_mov_b32_e32 v33, v15
	v_cndmask_b32_e64 v31, v32, v31, s[4:5]
	v_mov_b32_e32 v32, v15
	s_nop 1
	v_permlane32_swap_b32 v33, v32
	v_cndmask_b32_e64 v17, v30, v17, s[4:5]
	v_cndmask_b32_e64 v16, v16, v21, s[4:5]
	v_cndmask_b32_e64 v32, v32, v33, s[4:5]
	v_pk_mul_f32 v[16:17], v[136:137], v[16:17]
	v_mul_f32_e32 v21, v136, v31
	v_mov_b32_e32 v22, v240
	v_mov_b32_e32 v23, v241
	v_mov_b32_e32 v24, v242
	v_mov_b32_e32 v25, v243
	v_mov_b32_e32 v26, v244
	v_mov_b32_e32 v27, v245
	v_mov_b32_e32 v28, v246
	v_mov_b32_e32 v29, v247
	v_mul_f32_e32 v14, v14, v24
	v_pk_mul_f32 v[16:17], v[26:27], v[16:17]
	v_mul_f32_e32 v24, v28, v21
	v_mul_f32_e32 v27, v136, v32
	v_mov_b32_e32 v26, v15
	v_mov_b32_e32 v28, v25
	v_pk_mul_f32 v[26:27], v[26:27], v[28:29]
	v_pk_fma_f32 v[12:13], v[12:13], v[22:23], v[16:17]
	v_mov_b32_e32 v15, v26
	v_mov_b32_e32 v25, v27
	v_pk_add_f32 v[14:15], v[14:15], v[24:25]

.LBB0_1385:
	s_or_b64 exec, exec, s[0:1]
	s_and_saveexec_b64 s[0:1], s[8:9]
	s_cbranch_execz .LBB0_1387
	v_lshl_add_u64 v[12:13], v[18:19], 2, v[138:139]
	s_nop 0
	v_mov_b32_e32 v24, v6
	v_mov_b32_e32 v25, v6
	v_mov_b32_e32 v18, v4
	v_mov_b32_e32 v22, v4
	v_mov_b32_e32 v19, v5
	v_mov_b32_e32 v23, v5
	s_nop 1
	v_permlane32_swap_b32 v25, v24
	s_nop 1
	v_permlane32_swap_b32 v22, v18
	s_nop 1
	v_permlane32_swap_b32 v19, v23
	v_mov_b32_e32 v26, v7
	v_cndmask_b32_e64 v24, v24, v25, s[4:5]
	v_mov_b32_e32 v25, v7
	s_nop 1
	v_permlane32_swap_b32 v26, v25
	v_cndmask_b32_e64 v19, v23, v19, s[4:5]
	v_cndmask_b32_e64 v18, v18, v22, s[4:5]
	v_cndmask_b32_e64 v25, v25, v26, s[4:5]
	v_pk_mul_f32 v[18:19], v[136:137], v[18:19]
	v_mov_b32_e32 v8, v240
	v_mov_b32_e32 v9, v241
	v_mov_b32_e32 v10, v242
	v_mov_b32_e32 v11, v243
	v_mov_b32_e32 v12, v244
	v_mov_b32_e32 v13, v245
	v_mov_b32_e32 v14, v246
	v_mov_b32_e32 v15, v247
	v_mul_f32_e32 v6, v6, v10
	v_mul_f32_e32 v10, v136, v24
	v_pk_mul_f32 v[12:13], v[12:13], v[18:19]
	v_mul_f32_e32 v10, v14, v10
	v_mul_f32_e32 v19, v136, v25
	v_mov_b32_e32 v18, v7
	v_mov_b32_e32 v14, v11
	v_pk_mul_f32 v[14:15], v[18:19], v[14:15]
	v_pk_fma_f32 v[4:5], v[4:5], v[8:9], v[12:13]
	v_mov_b32_e32 v7, v14
	v_mov_b32_e32 v11, v15
	v_pk_add_f32 v[6:7], v[6:7], v[10:11]
